# MoE and dense GLU epilogues: packed f32 VALU ops replaced by their scalar halves (on top of v100)
# speedup vs baseline: 1.0113x; 1.0113x over previous
.LBB0_1472:
.LBB0_1473:
	v_exp_f32_e32 v2, v188
	v_exp_f32_e32 v3, v189
	v_mul_f32_e64 v6, v188, v156
	v_mul_f32_e64 v7, v189, v157
	v_exp_f32_e32 v8, v190
	v_exp_f32_e32 v9, v191
	v_add_f32_e64 v2, v2, 1.0
	v_add_f32_e64 v3, v3, 1.0
	v_exp_f32_e32 v10, v186
	v_rcp_f32_e32 v2, v2
	v_rcp_f32_e32 v3, v3
	v_add_f32_e64 v8, v8, 1.0
	v_add_f32_e64 v9, v9, 1.0
	v_exp_f32_e32 v11, v187
	v_rcp_f32_e32 v8, v8
	v_mul_f32_e64 v2, v2, v6
	v_mul_f32_e64 v3, v3, v7
	v_exp_f32_e32 v6, v184
	v_exp_f32_e32 v7, v185
	v_rcp_f32_e32 v9, v9
	v_mul_f32_e64 v4, v190, v158
	v_mul_f32_e64 v5, v191, v159
	v_readlane_b32 s14, v253, 61
	v_add_f32_e64 v6, v6, 1.0
	v_add_f32_e64 v7, v7, 1.0
	v_mul_f32_e64 v4, v8, v4
	v_mul_f32_e64 v5, v9, v5
	v_rcp_f32_e32 v6, v6
	v_rcp_f32_e32 v7, v7
	v_mul_f32_e64 v8, v184, v152
	v_mul_f32_e64 v9, v185, v153
	v_or_b32_e32 v1, s14, v1
	s_movk_i32 s14, 0xe00
	v_mul_f32_e64 v6, v6, v8
	v_mul_f32_e64 v7, v7, v9
	v_add_f32_e64 v8, v10, 1.0
	v_add_f32_e64 v9, v11, 1.0
	v_mul_lo_u32 v1, v1, s14
	v_rcp_f32_e32 v8, v8
	v_rcp_f32_e32 v9, v9
	v_cvt_pk_fp8_f32 v11, v6, v7
	v_cvt_pk_fp8_f32 v10, v2, v3
	v_mul_f32_e64 v2, v186, v154
	v_mul_f32_e64 v3, v187, v155
	v_mul_f32_e64 v6, v180, v148
	v_mul_f32_e64 v7, v181, v149
	v_mul_f32_e64 v2, v8, v2
	v_mul_f32_e64 v3, v9, v3
	v_exp_f32_e32 v8, v182
	v_cvt_pk_fp8_f32 v11, v2, v3 op_sel:[0,0,1]
	v_exp_f32_e32 v2, v180
	v_exp_f32_e32 v3, v181
	v_exp_f32_e32 v9, v183
	v_cvt_pk_fp8_f32 v10, v4, v5 op_sel:[0,0,1]
	v_lshlrev_b32_e32 v0, 3, v0
	v_add_f32_e64 v2, v2, 1.0
	v_add_f32_e64 v3, v3, 1.0
	v_readlane_b32 s14, v253, 63
	v_rcp_f32_e32 v2, v2
	v_rcp_f32_e32 v3, v3
	v_or3_b32 v0, v0, s14, v1
	s_mul_i32 s14, s55, 0xe00
	s_lshl_b32 s15, s97, 7
	v_mul_f32_e64 v2, v2, v6
	v_mul_f32_e64 v3, v3, v7
	v_exp_f32_e32 v6, v176
	v_exp_f32_e32 v7, v177
	v_add_f32_e64 v8, v8, 1.0
	v_add_f32_e64 v9, v9, 1.0
	s_add_i32 s14, s14, s15
	v_rcp_f32_e32 v8, v8
	v_rcp_f32_e32 v9, v9
	v_add_f32_e64 v6, v6, 1.0
	v_add_f32_e64 v7, v7, 1.0
	buffer_store_dwordx2 v[10:11], v0, s[8:11], s14 offen sc1
	v_rcp_f32_e32 v6, v6
	v_rcp_f32_e32 v7, v7
	v_exp_f32_e32 v10, v178
	v_exp_f32_e32 v11, v179
	v_mul_f32_e64 v4, v182, v150
	v_mul_f32_e64 v5, v183, v151
	s_add_i32 s15, s14, 0xe000
	v_mul_f32_e64 v4, v8, v4
	v_mul_f32_e64 v5, v9, v5
	v_mul_f32_e64 v8, v176, v144
	v_mul_f32_e64 v9, v177, v145
	s_or_b64 s[6:7], s[6:7], s[28:29]
	v_mul_f32_e64 v6, v6, v8
	v_mul_f32_e64 v7, v7, v9
	v_add_f32_e64 v8, v10, 1.0
	v_add_f32_e64 v9, v11, 1.0
	s_mov_b32 s64, s53
	v_rcp_f32_e32 v8, v8
	v_rcp_f32_e32 v9, v9
	v_cvt_pk_fp8_f32 v11, v6, v7
	v_cvt_pk_fp8_f32 v10, v2, v3
	v_mul_f32_e64 v2, v178, v146
	v_mul_f32_e64 v3, v179, v147
	v_mul_f32_e64 v6, v172, v140
	v_mul_f32_e64 v7, v173, v141
	v_mul_f32_e64 v2, v8, v2
	v_mul_f32_e64 v3, v9, v3
	v_exp_f32_e32 v8, v174
	v_cvt_pk_fp8_f32 v11, v2, v3 op_sel:[0,0,1]
	v_exp_f32_e32 v2, v172
	v_exp_f32_e32 v3, v173
	v_exp_f32_e32 v9, v175
	v_cvt_pk_fp8_f32 v10, v4, v5 op_sel:[0,0,1]
	v_mul_f32_e64 v4, v174, v142
	v_mul_f32_e64 v5, v175, v143
	v_add_f32_e64 v2, v2, 1.0
	v_add_f32_e64 v3, v3, 1.0
	v_add_f32_e64 v8, v8, 1.0
	v_add_f32_e64 v9, v9, 1.0
	v_rcp_f32_e32 v2, v2
	v_rcp_f32_e32 v3, v3
	v_rcp_f32_e32 v8, v8
	v_rcp_f32_e32 v9, v9
	buffer_store_dwordx2 v[10:11], v0, s[8:11], s15 offen sc1
	v_mul_f32_e64 v2, v2, v6
	v_mul_f32_e64 v3, v3, v7
	v_exp_f32_e32 v6, v168
	v_exp_f32_e32 v7, v169
	v_exp_f32_e32 v10, v170
	v_exp_f32_e32 v11, v171
	v_mul_f32_e64 v4, v8, v4
	v_mul_f32_e64 v5, v9, v5
	v_add_f32_e64 v6, v6, 1.0
	v_add_f32_e64 v7, v7, 1.0
	v_mul_f32_e64 v8, v168, v136
	v_mul_f32_e64 v9, v169, v137
	v_rcp_f32_e32 v6, v6
	v_rcp_f32_e32 v7, v7
	s_add_i32 s15, s14, 0x1c000
	v_mul_f32_e64 v6, v6, v8
	v_mul_f32_e64 v7, v7, v9
	v_add_f32_e64 v8, v10, 1.0
	v_add_f32_e64 v9, v11, 1.0
	s_nop 0
	v_rcp_f32_e32 v8, v8
	v_rcp_f32_e32 v9, v9
	v_cvt_pk_fp8_f32 v11, v6, v7
	v_cvt_pk_fp8_f32 v10, v2, v3
	v_mul_f32_e64 v2, v170, v138
	v_mul_f32_e64 v3, v171, v139
	v_mul_f32_e64 v6, v164, v132
	v_mul_f32_e64 v7, v165, v133
	v_mul_f32_e64 v2, v8, v2
	v_mul_f32_e64 v3, v9, v3
	v_exp_f32_e32 v8, v166
	v_cvt_pk_fp8_f32 v11, v2, v3 op_sel:[0,0,1]
	v_exp_f32_e32 v2, v164
	v_exp_f32_e32 v3, v165
	v_exp_f32_e32 v9, v167
	v_cvt_pk_fp8_f32 v10, v4, v5 op_sel:[0,0,1]
	v_mul_f32_e64 v4, v166, v134
	v_mul_f32_e64 v5, v167, v135
	v_add_f32_e64 v2, v2, 1.0
	v_add_f32_e64 v3, v3, 1.0
	v_add_f32_e64 v8, v8, 1.0
	v_add_f32_e64 v9, v9, 1.0
	v_rcp_f32_e32 v2, v2
	v_rcp_f32_e32 v3, v3
	v_rcp_f32_e32 v8, v8
	v_rcp_f32_e32 v9, v9
	buffer_store_dwordx2 v[10:11], v0, s[8:11], s15 offen sc1
	v_mul_f32_e64 v2, v2, v6
	v_mul_f32_e64 v3, v3, v7
	v_exp_f32_e32 v6, v160
	v_exp_f32_e32 v7, v161
	v_exp_f32_e32 v10, v162
	v_exp_f32_e32 v11, v163
	v_mul_f32_e64 v4, v8, v4
	v_mul_f32_e64 v5, v9, v5
	v_add_f32_e64 v6, v6, 1.0
	v_add_f32_e64 v7, v7, 1.0
	v_mul_f32_e64 v8, v160, v128
	v_mul_f32_e64 v9, v161, v129
	v_rcp_f32_e32 v6, v6
	v_rcp_f32_e32 v7, v7
	s_add_i32 s15, s14, 0x2a000
	v_mul_f32_e64 v6, v6, v8
	v_mul_f32_e64 v7, v7, v9
	v_add_f32_e64 v8, v10, 1.0
	v_add_f32_e64 v9, v11, 1.0
	s_nop 0
	v_rcp_f32_e32 v8, v8
	v_rcp_f32_e32 v9, v9
	v_cvt_pk_fp8_f32 v11, v6, v7
	v_cvt_pk_fp8_f32 v10, v2, v3
	v_mul_f32_e64 v2, v162, v130
	v_mul_f32_e64 v3, v163, v131
	v_mul_f32_e64 v6, v124, v92
	v_mul_f32_e64 v7, v125, v93
	v_mul_f32_e64 v2, v8, v2
	v_mul_f32_e64 v3, v9, v3
	v_exp_f32_e32 v8, v126
	v_cvt_pk_fp8_f32 v11, v2, v3 op_sel:[0,0,1]
	v_exp_f32_e32 v2, v124
	v_exp_f32_e32 v3, v125
	v_exp_f32_e32 v9, v127
	v_cvt_pk_fp8_f32 v10, v4, v5 op_sel:[0,0,1]
	v_mul_f32_e64 v4, v126, v94
	v_mul_f32_e64 v5, v127, v95
	v_add_f32_e64 v2, v2, 1.0
	v_add_f32_e64 v3, v3, 1.0
	v_add_f32_e64 v8, v8, 1.0
	v_add_f32_e64 v9, v9, 1.0
	v_rcp_f32_e32 v2, v2
	v_rcp_f32_e32 v3, v3
	v_rcp_f32_e32 v8, v8
	v_rcp_f32_e32 v9, v9
	buffer_store_dwordx2 v[10:11], v0, s[8:11], s15 offen sc1
	v_mul_f32_e64 v2, v2, v6
	v_mul_f32_e64 v3, v3, v7
	v_exp_f32_e32 v6, v120
	v_exp_f32_e32 v7, v121
	v_exp_f32_e32 v10, v122
	v_exp_f32_e32 v11, v123
	v_mul_f32_e64 v4, v8, v4
	v_mul_f32_e64 v5, v9, v5
	v_add_f32_e64 v6, v6, 1.0
	v_add_f32_e64 v7, v7, 1.0
	v_mul_f32_e64 v8, v120, v88
	v_mul_f32_e64 v9, v121, v89
	v_rcp_f32_e32 v6, v6
	v_rcp_f32_e32 v7, v7
	s_add_i32 s15, s14, 0x70000
	v_mul_f32_e64 v6, v6, v8
	v_mul_f32_e64 v7, v7, v9
	v_add_f32_e64 v8, v10, 1.0
	v_add_f32_e64 v9, v11, 1.0
	s_nop 0
	v_rcp_f32_e32 v8, v8
	v_rcp_f32_e32 v9, v9
	v_cvt_pk_fp8_f32 v11, v6, v7
	v_cvt_pk_fp8_f32 v10, v2, v3
	v_mul_f32_e64 v2, v122, v90
	v_mul_f32_e64 v3, v123, v91
	v_mul_f32_e64 v6, v116, v84
	v_mul_f32_e64 v7, v117, v85
	v_mul_f32_e64 v2, v8, v2
	v_mul_f32_e64 v3, v9, v3
	v_exp_f32_e32 v8, v118
	v_cvt_pk_fp8_f32 v11, v2, v3 op_sel:[0,0,1]
	v_exp_f32_e32 v2, v116
	v_exp_f32_e32 v3, v117
	v_exp_f32_e32 v9, v119
	v_cvt_pk_fp8_f32 v10, v4, v5 op_sel:[0,0,1]
	v_mul_f32_e64 v4, v118, v86
	v_mul_f32_e64 v5, v119, v87
	v_add_f32_e64 v2, v2, 1.0
	v_add_f32_e64 v3, v3, 1.0
	v_add_f32_e64 v8, v8, 1.0
	v_add_f32_e64 v9, v9, 1.0
	v_rcp_f32_e32 v2, v2
	v_rcp_f32_e32 v3, v3
	v_rcp_f32_e32 v8, v8
	v_rcp_f32_e32 v9, v9
	buffer_store_dwordx2 v[10:11], v0, s[8:11], s15 offen sc1
	v_mul_f32_e64 v2, v2, v6
	v_mul_f32_e64 v3, v3, v7
	v_exp_f32_e32 v6, v112
	v_exp_f32_e32 v7, v113
	v_exp_f32_e32 v10, v114
	v_exp_f32_e32 v11, v115
	v_mul_f32_e64 v4, v8, v4
	v_mul_f32_e64 v5, v9, v5
	v_add_f32_e64 v6, v6, 1.0
	v_add_f32_e64 v7, v7, 1.0
	v_mul_f32_e64 v8, v112, v80
	v_mul_f32_e64 v9, v113, v81
	v_rcp_f32_e32 v6, v6
	v_rcp_f32_e32 v7, v7
	s_add_i32 s15, s14, 0x7e000
	v_mul_f32_e64 v6, v6, v8
	v_mul_f32_e64 v7, v7, v9
	v_add_f32_e64 v8, v10, 1.0
	v_add_f32_e64 v9, v11, 1.0
	s_nop 0
	v_rcp_f32_e32 v8, v8
	v_rcp_f32_e32 v9, v9
	v_cvt_pk_fp8_f32 v11, v6, v7
	v_cvt_pk_fp8_f32 v10, v2, v3
	v_mul_f32_e64 v2, v114, v82
	v_mul_f32_e64 v3, v115, v83
	v_mul_f32_e64 v6, v108, v76
	v_mul_f32_e64 v7, v109, v77
	v_mul_f32_e64 v2, v8, v2
	v_mul_f32_e64 v3, v9, v3
	v_exp_f32_e32 v8, v110
	v_cvt_pk_fp8_f32 v11, v2, v3 op_sel:[0,0,1]
	v_exp_f32_e32 v2, v108
	v_exp_f32_e32 v3, v109
	v_exp_f32_e32 v9, v111
	v_cvt_pk_fp8_f32 v10, v4, v5 op_sel:[0,0,1]
	v_mul_f32_e64 v4, v110, v78
	v_mul_f32_e64 v5, v111, v79
	v_add_f32_e64 v2, v2, 1.0
	v_add_f32_e64 v3, v3, 1.0
	v_add_f32_e64 v8, v8, 1.0
	v_add_f32_e64 v9, v9, 1.0
	v_rcp_f32_e32 v2, v2
	v_rcp_f32_e32 v3, v3
	v_rcp_f32_e32 v8, v8
	v_rcp_f32_e32 v9, v9
	buffer_store_dwordx2 v[10:11], v0, s[8:11], s15 offen sc1
	v_mul_f32_e64 v2, v2, v6
	v_mul_f32_e64 v3, v3, v7
	v_exp_f32_e32 v6, v104
	v_exp_f32_e32 v7, v105
	v_exp_f32_e32 v10, v106
	v_exp_f32_e32 v11, v107
	v_mul_f32_e64 v4, v8, v4
	v_mul_f32_e64 v5, v9, v5
	v_add_f32_e64 v6, v6, 1.0
	v_add_f32_e64 v7, v7, 1.0
	v_mul_f32_e64 v8, v104, v72
	v_mul_f32_e64 v9, v105, v73
	v_rcp_f32_e32 v6, v6
	v_rcp_f32_e32 v7, v7
	s_add_i32 s15, s14, 0x8c000
	s_add_i32 s14, s14, 0x9a000
	s_cmp_gt_i32 s53, -1
	v_mul_f32_e64 v6, v6, v8
	v_mul_f32_e64 v7, v7, v9
	v_add_f32_e64 v8, v10, 1.0
	v_add_f32_e64 v9, v11, 1.0
	s_nop 0
	v_rcp_f32_e32 v8, v8
	v_rcp_f32_e32 v9, v9
	v_cvt_pk_fp8_f32 v11, v6, v7
	v_cvt_pk_fp8_f32 v10, v2, v3
	v_mul_f32_e64 v2, v106, v74
	v_mul_f32_e64 v3, v107, v75
	v_mul_f32_e64 v6, v100, v68
	v_mul_f32_e64 v7, v101, v69
	v_mul_f32_e64 v2, v8, v2
	v_mul_f32_e64 v3, v9, v3
	v_exp_f32_e32 v8, v102
	v_cvt_pk_fp8_f32 v11, v2, v3 op_sel:[0,0,1]
	v_exp_f32_e32 v2, v100
	v_exp_f32_e32 v3, v101
	v_exp_f32_e32 v9, v103
	v_cvt_pk_fp8_f32 v10, v4, v5 op_sel:[0,0,1]
	v_mul_f32_e64 v4, v102, v70
	v_mul_f32_e64 v5, v103, v71
	v_add_f32_e64 v2, v2, 1.0
	v_add_f32_e64 v3, v3, 1.0
	v_add_f32_e64 v8, v8, 1.0
	v_add_f32_e64 v9, v9, 1.0
	v_rcp_f32_e32 v2, v2
	v_rcp_f32_e32 v3, v3
	v_rcp_f32_e32 v8, v8
	v_rcp_f32_e32 v9, v9
	buffer_store_dwordx2 v[10:11], v0, s[8:11], s15 offen sc1
	v_mul_f32_e64 v2, v2, v6
	v_mul_f32_e64 v3, v3, v7
	v_exp_f32_e32 v6, v96
	v_exp_f32_e32 v7, v97
	v_exp_f32_e32 v10, v98
	v_exp_f32_e32 v11, v99
	v_mul_f32_e64 v4, v8, v4
	v_mul_f32_e64 v5, v9, v5
	v_add_f32_e64 v6, v6, 1.0
	v_add_f32_e64 v7, v7, 1.0
	v_mul_f32_e64 v8, v96, v64
	v_mul_f32_e64 v9, v97, v65
	v_rcp_f32_e32 v6, v6
	v_rcp_f32_e32 v7, v7
	s_nop 0
	v_mul_f32_e64 v6, v6, v8
	v_mul_f32_e64 v7, v7, v9
	v_add_f32_e64 v8, v10, 1.0
	v_add_f32_e64 v9, v11, 1.0
	s_nop 0
	v_rcp_f32_e32 v8, v8
	v_rcp_f32_e32 v9, v9
	v_cvt_pk_fp8_f32 v10, v2, v3
	v_cvt_pk_fp8_f32 v11, v6, v7
	v_mul_f32_e64 v2, v98, v66
	v_mul_f32_e64 v3, v99, v67
	v_cvt_pk_fp8_f32 v10, v4, v5 op_sel:[0,0,1]
	v_mul_f32_e64 v2, v8, v2
	v_mul_f32_e64 v3, v9, v3
	s_nop 0
	v_cvt_pk_fp8_f32 v11, v2, v3 op_sel:[0,0,1]
	buffer_store_dwordx2 v[10:11], v0, s[8:11], s14 offen sc1
	s_cselect_b64 s[14:15], -1, 0
	s_and_b64 s[6:7], s[6:7], s[14:15]
	s_andn2_b64 vcc, exec, s[6:7]
	s_cbranch_vccnz .LBB0_1478
	s_waitcnt vmcnt(0)
	s_and_saveexec_b64 s[6:7], s[2:3]
	s_cbranch_execz .LBB0_1477
	s_mov_b64 s[14:15], exec
	v_mbcnt_lo_u32_b32 v0, s14, 0
	v_mbcnt_hi_u32_b32 v0, s15, v0
	v_cmp_eq_u32_e32 vcc, 0, v0
	s_and_b64 s[22:23], exec, vcc
	s_mov_b64 exec, s[22:23]
	s_cbranch_execz .LBB0_1477
	s_lshl_b32 s64, s53, 6
	s_lshl_b64 s[22:23], s[64:65], 2
	s_add_u32 s22, s58, s22
	s_addc_u32 s23, s59, s23
	s_bcnt1_i32_b64 s14, s[14:15]
	v_mov_b32_e32 v0, s14
	global_atomic_add v209, v0, s[22:23]

.LBB0_1573:
	v_exp_f32_e32 v136, v124
	v_exp_f32_e32 v137, v125
	v_mul_f32_e64 v122, v126, v122
	v_mul_f32_e64 v123, v127, v123
	v_mul_f32_e64 v120, v124, v120
	v_mul_f32_e64 v121, v125, v121
	v_exp_f32_e32 v124, v126
	v_add_f32_e64 v136, v136, 1.0
	v_add_f32_e64 v137, v137, 1.0
	v_exp_f32_e32 v125, v127
	v_rcp_f32_e32 v136, v136
	v_rcp_f32_e32 v137, v137
	v_exp_f32_e32 v126, v116
	v_exp_f32_e32 v127, v117
	v_add_f32_e64 v124, v124, 1.0
	v_add_f32_e64 v125, v125, 1.0
	v_mul_f32_e64 v120, v136, v120
	v_mul_f32_e64 v121, v137, v121
	v_exp_f32_e32 v136, v118
	v_add_f32_e64 v126, v126, 1.0
	v_add_f32_e64 v127, v127, 1.0
	v_exp_f32_e32 v137, v119
	v_rcp_f32_e32 v124, v124
	v_rcp_f32_e32 v125, v125
	v_rcp_f32_e32 v126, v126
	v_rcp_f32_e32 v127, v127
	v_mov_b32_e32 v134, v128
	v_mul_f32_e64 v112, v116, v112
	v_mul_f32_e64 v113, v117, v113
	v_add_f32_e64 v116, v136, 1.0
	v_add_f32_e64 v117, v137, 1.0
	v_mul_f32_e64 v122, v124, v122
	v_mul_f32_e64 v123, v125, v123
	v_mul_f32_e64 v112, v126, v112
	v_mul_f32_e64 v113, v127, v113
	v_rcp_f32_e32 v116, v116
	v_rcp_f32_e32 v117, v117
	v_mul_f32_e64 v106, v110, v106
	v_mul_f32_e64 v107, v111, v107
	v_cvt_pk_fp8_f32 v125, v112, v113
	v_mul_f32_e64 v112, v118, v114
	v_mul_f32_e64 v113, v119, v115
	v_mul_f32_e64 v104, v108, v104
	v_mul_f32_e64 v105, v109, v105
	v_mul_f32_e64 v112, v116, v112
	v_mul_f32_e64 v113, v117, v113
	v_cvt_pk_fp8_f32 v124, v120, v121
	v_cvt_pk_fp8_f32 v125, v112, v113 op_sel:[0,0,1]
	v_exp_f32_e32 v112, v108
	v_exp_f32_e32 v113, v109
	v_exp_f32_e32 v108, v110
	v_exp_f32_e32 v109, v111
	v_exp_f32_e32 v110, v100
	v_add_f32_e64 v112, v112, 1.0
	v_add_f32_e64 v113, v113, 1.0
	v_exp_f32_e32 v111, v101
	v_rcp_f32_e32 v112, v112
	v_rcp_f32_e32 v113, v113
	v_add_f32_e64 v108, v108, 1.0
	v_add_f32_e64 v109, v109, 1.0
	v_add_f32_e64 v110, v110, 1.0
	v_add_f32_e64 v111, v111, 1.0
	v_cvt_pk_fp8_f32 v124, v122, v123 op_sel:[0,0,1]
	v_mul_f32_e64 v104, v112, v104
	v_mul_f32_e64 v105, v113, v105
	v_exp_f32_e32 v112, v102
	v_exp_f32_e32 v113, v103
	v_rcp_f32_e32 v108, v108
	v_rcp_f32_e32 v109, v109
	v_rcp_f32_e32 v110, v110
	v_rcp_f32_e32 v111, v111
	v_and_or_b32 v135, v134, 15, s28
	s_movk_i32 s6, 0xb00
	v_lshrrev_b32_e32 v134, 1, v134
	v_mul_lo_u32 v135, v135, s6
	v_and_b32_e32 v134, 24, v134
	s_mul_i32 s6, s10, 0xb00
	s_lshl_b32 s7, s11, 7
	v_or3_b32 v134, v135, v134, s29
	s_add_i32 s6, s7, s6
	s_mov_b32 s10, s62
	s_mov_b32 s11, s63
	v_mul_f32_e64 v92, v100, v92
	v_mul_f32_e64 v93, v101, v93
	v_add_f32_e64 v100, v112, 1.0
	v_add_f32_e64 v101, v113, 1.0
	buffer_store_dwordx2 v[124:125], v134, s[8:11], s6 offen
	v_mul_f32_e64 v106, v108, v106
	v_mul_f32_e64 v107, v109, v107
	v_mul_f32_e64 v92, v110, v92
	v_mul_f32_e64 v93, v111, v93
	v_rcp_f32_e32 v100, v100
	v_rcp_f32_e32 v101, v101
	v_mul_f32_e64 v88, v96, v88
	v_mul_f32_e64 v89, v97, v89
	v_cvt_pk_fp8_f32 v109, v92, v93
	v_mul_f32_e64 v92, v102, v94
	v_mul_f32_e64 v93, v103, v95
	v_cvt_pk_fp8_f32 v108, v104, v105
	v_mul_f32_e64 v92, v100, v92
	v_mul_f32_e64 v93, v101, v93
	s_add_i32 s7, s6, 0xb000
	v_cvt_pk_fp8_f32 v109, v92, v93 op_sel:[0,0,1]
	v_exp_f32_e32 v92, v96
	v_exp_f32_e32 v93, v97
	v_exp_f32_e32 v96, v86
	v_exp_f32_e32 v97, v87
	v_cvt_pk_fp8_f32 v108, v106, v107 op_sel:[0,0,1]
	v_add_f32_e64 v92, v92, 1.0
	v_add_f32_e64 v93, v93, 1.0
	v_mul_f32_e64 v76, v84, v76
	v_mul_f32_e64 v77, v85, v77
	v_rcp_f32_e32 v92, v92
	v_rcp_f32_e32 v93, v93
	buffer_store_dwordx2 v[108:109], v134, s[8:11], s7 offen
	v_exp_f32_e32 v94, v98
	v_exp_f32_e32 v95, v99
	v_mul_f32_e64 v88, v92, v88
	v_mul_f32_e64 v89, v93, v89
	v_exp_f32_e32 v92, v84
	v_exp_f32_e32 v93, v85
	v_add_f32_e64 v84, v96, 1.0
	v_add_f32_e64 v85, v97, 1.0
	v_add_f32_e64 v94, v94, 1.0
	v_add_f32_e64 v95, v95, 1.0
	v_rcp_f32_e32 v84, v84
	v_add_f32_e64 v92, v92, 1.0
	v_add_f32_e64 v93, v93, 1.0
	v_rcp_f32_e32 v85, v85
	v_rcp_f32_e32 v92, v92
	v_rcp_f32_e32 v93, v93
	v_mul_f32_e64 v72, v80, v72
	v_mul_f32_e64 v73, v81, v73
	v_rcp_f32_e32 v94, v94
	v_rcp_f32_e32 v95, v95
	v_mul_f32_e64 v76, v92, v76
	v_mul_f32_e64 v77, v93, v77
	v_mul_f32_e64 v90, v98, v90
	v_mul_f32_e64 v91, v99, v91
	v_cvt_pk_fp8_f32 v93, v76, v77
	v_mul_f32_e64 v76, v86, v78
	v_mul_f32_e64 v77, v87, v79
	v_cvt_pk_fp8_f32 v92, v88, v89
	v_mul_f32_e64 v76, v84, v76
	v_mul_f32_e64 v77, v85, v77
	v_mul_f32_e64 v90, v94, v90
	v_mul_f32_e64 v91, v95, v91
	v_cvt_pk_fp8_f32 v93, v76, v77 op_sel:[0,0,1]
	v_exp_f32_e32 v76, v80
	v_exp_f32_e32 v77, v81
	v_exp_f32_e32 v80, v70
	v_exp_f32_e32 v81, v71
	v_cvt_pk_fp8_f32 v92, v90, v91 op_sel:[0,0,1]
	v_add_f32_e64 v76, v76, 1.0
	v_add_f32_e64 v77, v77, 1.0
	s_add_i32 s7, s6, 0x16000
	v_rcp_f32_e32 v76, v76
	v_rcp_f32_e32 v77, v77
	v_mul_f32_e64 v64, v68, v64
	v_mul_f32_e64 v65, v69, v65
	buffer_store_dwordx2 v[92:93], v134, s[8:11], s7 offen
	v_exp_f32_e32 v78, v82
	v_mul_f32_e64 v72, v76, v72
	v_mul_f32_e64 v73, v77, v73
	v_exp_f32_e32 v76, v68
	v_exp_f32_e32 v77, v69
	v_add_f32_e64 v68, v80, 1.0
	v_add_f32_e64 v69, v81, 1.0
	v_exp_f32_e32 v79, v83
	v_rcp_f32_e32 v68, v68
	v_add_f32_e64 v76, v76, 1.0
	v_add_f32_e64 v77, v77, 1.0
	v_rcp_f32_e32 v69, v69
	v_rcp_f32_e32 v76, v76
	v_rcp_f32_e32 v77, v77
	v_add_f32_e64 v78, v78, 1.0
	v_add_f32_e64 v79, v79, 1.0
	v_mul_f32_e64 v58, v62, v58
	v_mul_f32_e64 v59, v63, v59
	v_rcp_f32_e32 v78, v78
	v_mul_f32_e64 v64, v76, v64
	v_mul_f32_e64 v65, v77, v65
	v_rcp_f32_e32 v79, v79
	v_cvt_pk_fp8_f32 v77, v64, v65
	v_mul_f32_e64 v64, v70, v66
	v_mul_f32_e64 v65, v71, v67
	v_mul_f32_e64 v56, v60, v56
	v_mul_f32_e64 v57, v61, v57
	v_mul_f32_e64 v64, v68, v64
	v_mul_f32_e64 v65, v69, v65
	v_cvt_pk_fp8_f32 v76, v72, v73
	v_cvt_pk_fp8_f32 v77, v64, v65 op_sel:[0,0,1]
	v_exp_f32_e32 v64, v60
	v_exp_f32_e32 v65, v61
	v_exp_f32_e32 v60, v62
	v_exp_f32_e32 v61, v63
	v_exp_f32_e32 v62, v52
	v_add_f32_e64 v64, v64, 1.0
	v_add_f32_e64 v65, v65, 1.0
	v_exp_f32_e32 v63, v53
	v_rcp_f32_e32 v64, v64
	v_rcp_f32_e32 v65, v65
	v_mul_f32_e64 v74, v82, v74
	v_mul_f32_e64 v75, v83, v75
	v_add_f32_e64 v60, v60, 1.0
	v_add_f32_e64 v61, v61, 1.0
	v_mul_f32_e64 v74, v78, v74
	v_mul_f32_e64 v75, v79, v75
	v_mul_f32_e64 v56, v64, v56
	v_mul_f32_e64 v57, v65, v57
	v_add_f32_e64 v62, v62, 1.0
	v_add_f32_e64 v63, v63, 1.0
	v_exp_f32_e32 v64, v54
	v_exp_f32_e32 v65, v55
	v_cvt_pk_fp8_f32 v76, v74, v75 op_sel:[0,0,1]
	v_rcp_f32_e32 v60, v60
	v_rcp_f32_e32 v61, v61
	v_rcp_f32_e32 v62, v62
	v_rcp_f32_e32 v63, v63
	s_add_i32 s7, s6, 0x21000
	v_mul_f32_e64 v44, v52, v44
	v_mul_f32_e64 v45, v53, v45
	v_add_f32_e64 v52, v64, 1.0
	v_add_f32_e64 v53, v65, 1.0
	buffer_store_dwordx2 v[76:77], v134, s[8:11], s7 offen
	v_mul_f32_e64 v58, v60, v58
	v_mul_f32_e64 v59, v61, v59
	v_mul_f32_e64 v44, v62, v44
	v_mul_f32_e64 v45, v63, v45
	v_rcp_f32_e32 v52, v52
	v_rcp_f32_e32 v53, v53
	v_mul_f32_e64 v40, v48, v40
	v_mul_f32_e64 v41, v49, v41
	v_cvt_pk_fp8_f32 v61, v44, v45
	v_mul_f32_e64 v44, v54, v46
	v_mul_f32_e64 v45, v55, v47
	v_cvt_pk_fp8_f32 v60, v56, v57
	v_mul_f32_e64 v44, v52, v44
	v_mul_f32_e64 v45, v53, v45
	s_add_i32 s7, s6, 0x58000
	v_cvt_pk_fp8_f32 v61, v44, v45 op_sel:[0,0,1]
	v_exp_f32_e32 v44, v48
	v_exp_f32_e32 v45, v49
	v_exp_f32_e32 v48, v38
	v_exp_f32_e32 v49, v39
	v_cvt_pk_fp8_f32 v60, v58, v59 op_sel:[0,0,1]
	v_add_f32_e64 v44, v44, 1.0
	v_add_f32_e64 v45, v45, 1.0
	v_mul_f32_e64 v28, v36, v28
	v_mul_f32_e64 v29, v37, v29
	v_rcp_f32_e32 v44, v44
	v_rcp_f32_e32 v45, v45
	buffer_store_dwordx2 v[60:61], v134, s[8:11], s7 offen
	v_exp_f32_e32 v46, v50
	v_exp_f32_e32 v47, v51
	v_mul_f32_e64 v40, v44, v40
	v_mul_f32_e64 v41, v45, v41
	v_exp_f32_e32 v44, v36
	v_exp_f32_e32 v45, v37
	v_add_f32_e64 v36, v48, 1.0
	v_add_f32_e64 v37, v49, 1.0
	v_add_f32_e64 v46, v46, 1.0
	v_add_f32_e64 v47, v47, 1.0
	v_rcp_f32_e32 v36, v36
	v_add_f32_e64 v44, v44, 1.0
	v_add_f32_e64 v45, v45, 1.0
	v_rcp_f32_e32 v37, v37
	v_rcp_f32_e32 v44, v44
	v_rcp_f32_e32 v45, v45
	v_mul_f32_e64 v24, v32, v24
	v_mul_f32_e64 v25, v33, v25
	v_rcp_f32_e32 v46, v46
	v_rcp_f32_e32 v47, v47
	v_mul_f32_e64 v28, v44, v28
	v_mul_f32_e64 v29, v45, v29
	v_mul_f32_e64 v42, v50, v42
	v_mul_f32_e64 v43, v51, v43
	v_cvt_pk_fp8_f32 v45, v28, v29
	v_mul_f32_e64 v28, v38, v30
	v_mul_f32_e64 v29, v39, v31
	v_cvt_pk_fp8_f32 v44, v40, v41
	v_mul_f32_e64 v28, v36, v28
	v_mul_f32_e64 v29, v37, v29
	v_mul_f32_e64 v42, v46, v42
	v_mul_f32_e64 v43, v47, v43
	v_cvt_pk_fp8_f32 v45, v28, v29 op_sel:[0,0,1]
	v_exp_f32_e32 v28, v32
	v_exp_f32_e32 v29, v33
	v_exp_f32_e32 v32, v22
	v_exp_f32_e32 v33, v23
	v_cvt_pk_fp8_f32 v44, v42, v43 op_sel:[0,0,1]
	v_add_f32_e64 v28, v28, 1.0
	v_add_f32_e64 v29, v29, 1.0
	s_add_i32 s7, s6, 0x63000
	v_rcp_f32_e32 v28, v28
	v_rcp_f32_e32 v29, v29
	v_mul_f32_e64 v12, v20, v12
	v_mul_f32_e64 v13, v21, v13
	buffer_store_dwordx2 v[44:45], v134, s[8:11], s7 offen
	v_exp_f32_e32 v30, v34
	v_mul_f32_e64 v24, v28, v24
	v_mul_f32_e64 v25, v29, v25
	v_exp_f32_e32 v28, v20
	v_exp_f32_e32 v29, v21
	v_add_f32_e64 v20, v32, 1.0
	v_add_f32_e64 v21, v33, 1.0
	v_exp_f32_e32 v31, v35
	v_rcp_f32_e32 v20, v20
	v_add_f32_e64 v28, v28, 1.0
	v_add_f32_e64 v29, v29, 1.0
	v_rcp_f32_e32 v21, v21
	v_rcp_f32_e32 v28, v28
	v_rcp_f32_e32 v29, v29
	v_add_f32_e64 v30, v30, 1.0
	v_add_f32_e64 v31, v31, 1.0
	v_mul_f32_e64 v8, v16, v8
	v_mul_f32_e64 v9, v17, v9
	v_rcp_f32_e32 v30, v30
	v_mul_f32_e64 v12, v28, v12
	v_mul_f32_e64 v13, v29, v13
	v_rcp_f32_e32 v31, v31
	v_cvt_pk_fp8_f32 v29, v12, v13
	v_mul_f32_e64 v12, v22, v14
	v_mul_f32_e64 v13, v23, v15
	v_cvt_pk_fp8_f32 v28, v24, v25
	v_mul_f32_e64 v12, v20, v12
	v_mul_f32_e64 v13, v21, v13
	v_mul_f32_e64 v26, v34, v26
	v_mul_f32_e64 v27, v35, v27
	v_cvt_pk_fp8_f32 v29, v12, v13 op_sel:[0,0,1]
	v_exp_f32_e32 v12, v16
	v_exp_f32_e32 v13, v17
	v_mul_f32_e64 v26, v30, v26
	v_mul_f32_e64 v27, v31, v27
	v_exp_f32_e32 v14, v18
	v_exp_f32_e32 v15, v19
	v_add_f32_e64 v12, v12, 1.0
	v_add_f32_e64 v13, v13, 1.0
	v_exp_f32_e32 v16, v6
	v_rcp_f32_e32 v12, v12
	v_rcp_f32_e32 v13, v13
	v_exp_f32_e32 v17, v7
	v_cvt_pk_fp8_f32 v28, v26, v27 op_sel:[0,0,1]
	s_add_i32 s7, s6, 0x6e000
	v_mul_f32_e64 v8, v12, v8
	v_mul_f32_e64 v9, v13, v9
	v_exp_f32_e32 v12, v4
	v_exp_f32_e32 v13, v5
	v_add_f32_e64 v14, v14, 1.0
	v_add_f32_e64 v15, v15, 1.0
	v_mul_f32_e64 v0, v4, v0
	v_mul_f32_e64 v1, v5, v1
	v_add_f32_e64 v4, v16, 1.0
	v_add_f32_e64 v5, v17, 1.0
	v_add_f32_e64 v12, v12, 1.0
	v_add_f32_e64 v13, v13, 1.0
	buffer_store_dwordx2 v[28:29], v134, s[8:11], s7 offen
	v_rcp_f32_e32 v12, v12
	v_rcp_f32_e32 v13, v13
	v_rcp_f32_e32 v14, v14
	v_rcp_f32_e32 v15, v15
	v_rcp_f32_e32 v4, v4
	v_mul_f32_e64 v0, v12, v0
	v_mul_f32_e64 v1, v13, v1
	v_rcp_f32_e32 v5, v5
	v_mul_f32_e64 v10, v18, v10
	v_mul_f32_e64 v11, v19, v11
	v_cvt_pk_fp8_f32 v12, v8, v9
	v_cvt_pk_fp8_f32 v13, v0, v1
	v_mul_f32_e64 v0, v6, v2
	v_mul_f32_e64 v1, v7, v3
	v_mul_f32_e64 v10, v14, v10
	v_mul_f32_e64 v11, v15, v11
	v_mul_f32_e64 v0, v4, v0
	v_mul_f32_e64 v1, v5, v1
	v_cvt_pk_fp8_f32 v12, v10, v11 op_sel:[0,0,1]
	v_cvt_pk_fp8_f32 v13, v0, v1 op_sel:[0,0,1]
	s_add_i32 s6, s6, 0x79000
	s_andn2_b64 vcc, exec, s[0:1]
	s_mov_b64 s[0:1], -1
	v_readlane_b32 s48, v253, 48
	buffer_store_dwordx2 v[12:13], v134, s[8:11], s6 offen
	s_cbranch_vccnz .LBB0_1566
	s_andn2_b64 vcc, exec, s[2:3]
	s_cbranch_vccnz .LBB0_1565
	s_barrier
	s_branch .LBB0_1565
